# baseline (speedup 1.0000x reference)
_Z15zero_cnt_kernelPy:
	v_cmp_gt_u32_e32 vcc, 8, v0
	s_and_saveexec_b64 s[2:3], vcc
	s_cbranch_execz .LBB0_2
	s_load_dwordx2 s[0:1], s[0:1], 0x0
	v_lshlrev_b32_e32 v2, 7, v0
	v_mov_b32_e32 v0, 0
	v_mov_b32_e32 v1, v0
	s_waitcnt lgkmcnt(0)
	global_store_dwordx2 v2, v[0:1], s[0:1] sc1
